# combination variant plus adaLN unit remap (adjacent 64-byte column blocks handled by two waves of the same workgroup)
# baseline (speedup 1.0000x reference)
.LBB0_16:
	v_writelane_b32 v251, s36, 28
	s_nop 1
	v_writelane_b32 v251, s37, 29
	v_writelane_b32 v251, s38, 30
	v_writelane_b32 v251, s39, 31
	v_writelane_b32 v251, s40, 32
	v_writelane_b32 v251, s41, 33
	v_writelane_b32 v251, s42, 34
	v_writelane_b32 v251, s43, 35
	v_writelane_b32 v251, s44, 36
	v_writelane_b32 v251, s45, 37
	v_writelane_b32 v251, s46, 38
	v_writelane_b32 v251, s47, 39
	v_writelane_b32 v251, s48, 40
	v_writelane_b32 v251, s49, 41
	v_writelane_b32 v251, s50, 42
	v_writelane_b32 v251, s51, 43
	s_or_b64 exec, exec, s[2:3]
	s_load_dwordx16 s[52:67], s[0:1], 0x40
	s_load_dwordx16 s[36:51], s[0:1], 0x80
	v_mov_b32_e32 v0, 0x5ff
	v_readlane_b32 s22, v251, 20
	s_lshr_b32 s23, s22, 1
	s_and_b32 s22, s22, 1
	s_lshl_b32 s23, s23, 9
	s_add_i32 s22, s22, s23
	v_readlane_b32 s23, v251, 4
	s_lshl_b32 s23, s23, 1
	s_add_i32 s22, s22, s23
	s_nop 1
	v_cmp_gt_i32_e32 vcc, s22, v0
	v_and_b32_e32 v1, 63, v50
	v_mbcnt_lo_u32_b32 v51, -1, 0
	s_waitcnt lgkmcnt(0)
	v_writelane_b32 v251, s36, 44
	s_barrier
	s_nop 0
	v_writelane_b32 v251, s37, 45
	v_writelane_b32 v251, s38, 46
	v_writelane_b32 v251, s39, 47
	v_writelane_b32 v251, s40, 48
	v_writelane_b32 v251, s41, 49
	v_writelane_b32 v251, s42, 50
	v_writelane_b32 v251, s43, 51
	v_writelane_b32 v251, s44, 52
	v_writelane_b32 v251, s45, 53
	v_writelane_b32 v251, s46, 54
	v_writelane_b32 v251, s47, 55
	v_writelane_b32 v251, s48, 56
	v_writelane_b32 v251, s49, 57
	v_writelane_b32 v251, s50, 58
	v_writelane_b32 v251, s51, 59
	s_nop 0
	v_readlane_b32 s0, v251, 5
	v_readlane_b32 s6, v251, 11
	v_readlane_b32 s1, v251, 6
	v_readlane_b32 s7, v251, 12
	s_add_u32 s0, s6, 0x100000
	s_addc_u32 s1, s7, 0
	v_readlane_b32 s2, v251, 7
	v_readlane_b32 s3, v251, 8
	v_readlane_b32 s4, v251, 9
	v_readlane_b32 s5, v251, 10
	v_writelane_b32 v251, s0, 26
	s_nop 1
	v_writelane_b32 v251, s1, 27
	s_and_b64 s[0:1], vcc, exec
	s_cbranch_scc1 .LBB0_23
	v_lshlrev_b32_e32 v0, 4, v1
	v_and_b32_e32 v0, 0x300, v0
	v_readlane_b32 s36, v251, 28
	v_mul_u32_u24_e32 v46, 0x6000, v0
	v_mov_b32_e32 v47, 0
	v_readlane_b32 s44, v251, 36
	v_readlane_b32 s45, v251, 37
	v_and_b32_e32 v62, 15, v50
	s_movk_i32 s4, 0x6000
	v_lshl_add_u64 v[48:49], s[44:45], 0, v[46:47]
	v_lshl_add_u32 v46, v0, 2, 0
	v_mbcnt_hi_u32_b32 v0, -1, v51
	v_and_b32_e32 v3, 64, v0
	v_xor_b32_e32 v2, 16, v0
	v_add_u32_e32 v3, 64, v3
	v_cmp_lt_i32_e32 vcc, v2, v3
	v_cmp_gt_u32_e64 s[0:1], 16, v1
	v_mov_b32_e32 v65, 0x1800000
	v_cndmask_b32_e32 v2, v0, v2, vcc
	v_lshlrev_b32_e32 v63, 2, v2
	v_xor_b32_e32 v2, 32, v0
	v_cmp_lt_i32_e32 vcc, v2, v3
	s_mov_b32 s5, 0xc000
	s_mov_b32 s6, 0x12000
	v_cndmask_b32_e32 v0, v0, v2, vcc
	v_lshlrev_b32_e32 v64, 2, v0
	s_mov_b32 s7, 0x18000
	s_mov_b32 s9, 0x1e000
	s_mov_b32 s10, 0x24000
	s_mov_b32 s11, 0x2a000
	s_mov_b32 s12, 0x30000
	s_mov_b32 s13, 0x36000
	s_mov_b32 s14, 0x3c000
	s_mov_b32 s15, 0x42000
	s_mov_b32 s18, 0x48000
	s_mov_b32 s19, 0x4e000
	s_mov_b32 s20, 0x54000
	s_mov_b32 s21, 0x5a000
	v_readlane_b32 s37, v251, 29
	v_readlane_b32 s38, v251, 30
	v_readlane_b32 s39, v251, 31
	v_readlane_b32 s40, v251, 32
	v_readlane_b32 s41, v251, 33
	v_readlane_b32 s42, v251, 34
	v_readlane_b32 s43, v251, 35
	v_readlane_b32 s46, v251, 38
	v_readlane_b32 s47, v251, 39
	v_readlane_b32 s48, v251, 40
	v_readlane_b32 s49, v251, 41
	v_readlane_b32 s50, v251, 42
	v_readlane_b32 s51, v251, 43
	s_branch .LBB0_19
